# grid barrier: leaders wait on the top arrival counter reaching (generation+1)*nXCD; separate generation publish removed
# speedup vs baseline: 1.0019x; 1.0019x over previous
; __device__ __forceinline__ unsigned xb_ld(unsigned* p)              { return __hip_atomic_load(p, __ATOMIC_RELAXED, __HIP_MEMORY_SCOPE_AGENT); }
; __device__ __forceinline__ unsigned xb_add(unsigned* p, unsigned v) { return __hip_atomic_fetch_add(p, v, __ATOMIC_RELAXED, __HIP_MEMORY_SCOPE_AGENT); }
; #define XB_SPIN(cond, bar) do { unsigned _sp = 0; while (cond) { __builtin_amdgcn_s_sleep(1); \
;     if ((++_sp & 255u) == 0u) { if (xb_ld(&(bar)[XB_TMO])) break; if (_sp > XB_SPIN_CAP) { atomicAdd(&(bar)[XB_TMO], 1u); break; } } } } while (0)
; __device__ __forceinline__ void xcd_barrier(const XcdBarrier& b) {
;     ...
;         const unsigned old = xb_add(&bar[XB_XSUB(b.x)], 1u);
;         const unsigned gen = old / nloc;
;         if (old + 1u == (gen + 1u) * nloc) {
;             __builtin_amdgcn_fence(__ATOMIC_RELEASE, "agent");
;             asm volatile("s_waitcnt vmcnt(0)" ::: "memory");
;             const unsigned og = xb_add(&bar[XB_TOP], 1u);
;             const unsigned tg = og / nx;
;             if (og + 1u == (tg + 1u) * nx) xb_add(&bar[XB_TOPGEN], 1u);
;             else XB_SPIN(xb_ld(&bar[XB_TOPGEN]) == tg, bar);
;             __builtin_amdgcn_fence(__ATOMIC_ACQUIRE, "agent");
;             xb_add(&bar[XB_XGEN(b.x)], 1u);
;             asm volatile("s_waitcnt vmcnt(0)" ::: "memory");
.LBB0_159:
	s_or_b64 exec, exec, s[12:13]
	v_cvt_f32_u32_e32 v4, v2
	s_waitcnt vmcnt(0)
	v_readfirstlane_b32 s3, v3
	v_sub_u32_e32 v3, 0, v2
	v_rcp_iflag_f32_e32 v4, v4
	v_add_u32_e32 v5, s3, v1
	v_mul_f32_e32 v4, 0x4f7ffffe, v4
	v_cvt_u32_f32_e32 v4, v4
	v_mul_lo_u32 v1, v3, v4
	v_mul_hi_u32 v1, v4, v1
	v_add_u32_e32 v1, v4, v1
	v_mul_hi_u32 v1, v5, v1
	v_mul_lo_u32 v3, v1, v2
	v_sub_u32_e32 v3, v5, v3
	v_add_u32_e32 v4, 1, v1
	v_cmp_ge_u32_e32 vcc, v3, v2
	s_nop 1
	v_cndmask_b32_e32 v1, v1, v4, vcc
	v_sub_u32_e32 v4, v3, v2
	v_cndmask_b32_e32 v3, v3, v4, vcc
	v_add_u32_e32 v4, 1, v1
	v_cmp_ge_u32_e32 vcc, v3, v2
	v_add_u32_e32 v3, 1, v5
	s_nop 0
	v_cndmask_b32_e32 v1, v1, v4, vcc
	v_mul_lo_u32 v4, v2, v1
	v_add_u32_e32 v2, v4, v2
	v_cmp_ne_u32_e32 vcc, v3, v2
	s_and_saveexec_b64 s[10:11], vcc
	s_xor_b64 s[10:11], exec, s[10:11]
	s_cbranch_execz .LBB0_173
	s_waitcnt lgkmcnt(0)
	v_mad_u32_u24 v3, v1, v0, v0
	v_mov_b32_e32 v0, 0x3400
	global_load_dword v0, v0, s[30:31] sc1
	s_add_u32 s14, s30, 0x3400
	s_addc_u32 s15, s31, 0
	s_waitcnt vmcnt(0)
	v_cmp_lt_u32_e32 vcc, v0, v3
	s_and_saveexec_b64 s[12:13], vcc
	s_cbranch_execz .LBB0_172
	s_mov_b32 s3, 1
	s_mov_b64 s[16:17], 0
	v_mov_b32_e32 v0, 0
	s_branch .LBB0_163

; __device__ __forceinline__ unsigned xb_ld(unsigned* p)              { return __hip_atomic_load(p, __ATOMIC_RELAXED, __HIP_MEMORY_SCOPE_AGENT); }
; #define XB_SPIN(cond, bar) do { unsigned _sp = 0; while (cond) { __builtin_amdgcn_s_sleep(1); \
;     if ((++_sp & 255u) == 0u) { if (xb_ld(&(bar)[XB_TMO])) break; if (_sp > XB_SPIN_CAP) { atomicAdd(&(bar)[XB_TMO], 1u); break; } } } } while (0)
; __device__ __forceinline__ void xcd_barrier(const XcdBarrier& b) {
;     ...
;             else XB_SPIN(xb_ld(&bar[XB_TOPGEN]) == tg, bar);
.LBB0_167:
	global_load_dword v2, v0, s[14:15] sc1
	s_add_i32 s3, s3, 1
	s_mov_b64 s[22:23], -1
	s_waitcnt vmcnt(0)
	v_cmp_ge_u32_e32 vcc, v2, v3
	s_orn2_b64 s[20:21], vcc, exec
	s_branch .LBB0_162

; __device__ __forceinline__ unsigned xb_ld(unsigned* p)              { return __hip_atomic_load(p, __ATOMIC_RELAXED, __HIP_MEMORY_SCOPE_AGENT); }
; __device__ __forceinline__ unsigned xb_add(unsigned* p, unsigned v) { return __hip_atomic_fetch_add(p, v, __ATOMIC_RELAXED, __HIP_MEMORY_SCOPE_AGENT); }
; #define XB_SPIN(cond, bar) do { unsigned _sp = 0; while (cond) { __builtin_amdgcn_s_sleep(1); \
;     if ((++_sp & 255u) == 0u) { if (xb_ld(&(bar)[XB_TMO])) break; if (_sp > XB_SPIN_CAP) { atomicAdd(&(bar)[XB_TMO], 1u); break; } } } } while (0)
; __device__ __forceinline__ void xcd_barrier(const XcdBarrier& b) {
;     ...
;         const unsigned old = xb_add(&bar[XB_XSUB(b.x)], 1u);
;         const unsigned gen = old / nloc;
;         if (old + 1u == (gen + 1u) * nloc) {
;             __builtin_amdgcn_fence(__ATOMIC_RELEASE, "agent");
;             asm volatile("s_waitcnt vmcnt(0)" ::: "memory");
;             const unsigned og = xb_add(&bar[XB_TOP], 1u);
;             const unsigned tg = og / nx;
;             if (og + 1u == (tg + 1u) * nx) xb_add(&bar[XB_TOPGEN], 1u);
;             else XB_SPIN(xb_ld(&bar[XB_TOPGEN]) == tg, bar);
;             __builtin_amdgcn_fence(__ATOMIC_ACQUIRE, "agent");
;             xb_add(&bar[XB_XGEN(b.x)], 1u);
;             asm volatile("s_waitcnt vmcnt(0)" ::: "memory");
.LBB0_176:
	s_or_b64 exec, exec, s[12:13]
	v_cvt_f32_u32_e32 v3, v0
	s_waitcnt vmcnt(0)
	v_readfirstlane_b32 s3, v2
	s_add_u32 s12, s30, 0x3400
	s_addc_u32 s13, s31, 0
	v_rcp_iflag_f32_e32 v3, v3
	v_add_u32_e32 v1, s3, v1
	v_add_u32_e32 v4, 1, v1
	s_mov_b64 s[14:15], -1
	v_mul_f32_e32 v2, 0x4f7ffffe, v3
	v_cvt_u32_f32_e32 v2, v2
	v_sub_u32_e32 v3, 0, v0
	v_mul_lo_u32 v3, v3, v2
	v_mul_hi_u32 v3, v2, v3
	v_add_u32_e32 v2, v2, v3
	v_mul_hi_u32 v2, v1, v2
	v_mul_lo_u32 v3, v2, v0
	v_sub_u32_e32 v1, v1, v3
	v_add_u32_e32 v5, 1, v2
	v_cmp_ge_u32_e32 vcc, v1, v0
	v_sub_u32_e32 v3, v1, v0
	s_nop 0
	v_cndmask_b32_e32 v2, v2, v5, vcc
	v_cndmask_b32_e32 v1, v1, v3, vcc
	v_add_u32_e32 v3, 1, v2
	v_cmp_ge_u32_e32 vcc, v1, v0
	s_nop 1
	v_cndmask_b32_e32 v2, v2, v3, vcc
	v_mul_lo_u32 v1, v0, v2
	v_add_u32_e32 v0, v1, v0
	v_mov_b32_e32 v6, v0
	v_cmp_ne_u32_e32 vcc, v4, v0
	v_mov_b64_e32 v[0:1], s[12:13]
	s_and_saveexec_b64 s[10:11], vcc
	s_cbranch_execz .LBB0_188
	v_mov_b32_e32 v0, 0
	global_load_dword v1, v0, s[12:13] sc1
	s_mov_b64 s[18:19], 0
	s_waitcnt vmcnt(0)
	v_cmp_lt_u32_e32 vcc, v1, v6
	s_and_saveexec_b64 s[16:17], vcc
	s_cbranch_execz .LBB0_187
	s_add_u32 s14, s30, 0x200
	s_addc_u32 s15, s31, 0
	s_mov_b32 s3, 1
	s_branch .LBB0_180

; __device__ __forceinline__ unsigned xb_ld(unsigned* p)              { return __hip_atomic_load(p, __ATOMIC_RELAXED, __HIP_MEMORY_SCOPE_AGENT); }
; #define XB_SPIN(cond, bar) do { unsigned _sp = 0; while (cond) { __builtin_amdgcn_s_sleep(1); \
;     if ((++_sp & 255u) == 0u) { if (xb_ld(&(bar)[XB_TMO])) break; if (_sp > XB_SPIN_CAP) { atomicAdd(&(bar)[XB_TMO], 1u); break; } } } } while (0)
; __device__ __forceinline__ void xcd_barrier(const XcdBarrier& b) {
;     ...
;             else XB_SPIN(xb_ld(&bar[XB_TOPGEN]) == tg, bar);
.LBB0_184:
	global_load_dword v1, v0, s[12:13] sc1
	s_add_i32 s3, s3, 1
	s_mov_b64 s[22:23], -1
	s_waitcnt vmcnt(0)
	v_cmp_ge_u32_e32 vcc, v1, v6
	s_orn2_b64 s[26:27], vcc, exec
	s_branch .LBB0_179

; __device__ __forceinline__ unsigned xb_ld(unsigned* p)              { return __hip_atomic_load(p, __ATOMIC_RELAXED, __HIP_MEMORY_SCOPE_AGENT); }
; __device__ __forceinline__ unsigned xb_add(unsigned* p, unsigned v) { return __hip_atomic_fetch_add(p, v, __ATOMIC_RELAXED, __HIP_MEMORY_SCOPE_AGENT); }
; #define XB_SPIN(cond, bar) do { unsigned _sp = 0; while (cond) { __builtin_amdgcn_s_sleep(1); \
;     if ((++_sp & 255u) == 0u) { if (xb_ld(&(bar)[XB_TMO])) break; if (_sp > XB_SPIN_CAP) { atomicAdd(&(bar)[XB_TMO], 1u); break; } } } } while (0)
; __device__ __forceinline__ void xcd_barrier(const XcdBarrier& b) {
;     ...
;             const unsigned og = xb_add(&bar[XB_TOP], 1u);
;             const unsigned tg = og / nx;
;             if (og + 1u == (tg + 1u) * nx) xb_add(&bar[XB_TOPGEN], 1u);
;             else XB_SPIN(xb_ld(&bar[XB_TOPGEN]) == tg, bar);
;             __builtin_amdgcn_fence(__ATOMIC_ACQUIRE, "agent");
;             xb_add(&bar[XB_XGEN(b.x)], 1u);
.LBB0_188:
	s_or_b64 exec, exec, s[10:11]
	s_and_saveexec_b64 s[10:11], s[14:15]
	s_cbranch_execz .LBB0_190
.LBB0_190:
	s_or_b64 exec, exec, s[10:11]
	s_waitcnt vmcnt(0)
	buffer_inv sc1
	s_waitcnt vmcnt(0)

; __device__ __forceinline__ unsigned xb_ld(unsigned* p)              { return __hip_atomic_load(p, __ATOMIC_RELAXED, __HIP_MEMORY_SCOPE_AGENT); }
; __device__ __forceinline__ unsigned xb_add(unsigned* p, unsigned v) { return __hip_atomic_fetch_add(p, v, __ATOMIC_RELAXED, __HIP_MEMORY_SCOPE_AGENT); }
; #define XB_SPIN(cond, bar) do { unsigned _sp = 0; while (cond) { __builtin_amdgcn_s_sleep(1); \
;     if ((++_sp & 255u) == 0u) { if (xb_ld(&(bar)[XB_TMO])) break; if (_sp > XB_SPIN_CAP) { atomicAdd(&(bar)[XB_TMO], 1u); break; } } } } while (0)
; __device__ __forceinline__ void xcd_barrier(const XcdBarrier& b) {
;     ...
;             const unsigned og = xb_add(&bar[XB_TOP], 1u);
;             const unsigned tg = og / nx;
;             if (og + 1u == (tg + 1u) * nx) xb_add(&bar[XB_TOPGEN], 1u);
;             else XB_SPIN(xb_ld(&bar[XB_TOPGEN]) == tg, bar);
;             __builtin_amdgcn_fence(__ATOMIC_ACQUIRE, "agent");
;             xb_add(&bar[XB_XGEN(b.x)], 1u);
.LBB0_353:
	s_or_b64 exec, exec, s[10:11]
	s_and_saveexec_b64 s[10:11], s[14:15]
	s_cbranch_execz .LBB0_355
.LBB0_355:
	s_or_b64 exec, exec, s[10:11]
	s_waitcnt vmcnt(0)
	buffer_inv sc1
	s_waitcnt vmcnt(0)

; __device__ __forceinline__ unsigned xb_ld(unsigned* p)              { return __hip_atomic_load(p, __ATOMIC_RELAXED, __HIP_MEMORY_SCOPE_AGENT); }
; __device__ __forceinline__ unsigned xb_add(unsigned* p, unsigned v) { return __hip_atomic_fetch_add(p, v, __ATOMIC_RELAXED, __HIP_MEMORY_SCOPE_AGENT); }
; #define XB_SPIN(cond, bar) do { unsigned _sp = 0; while (cond) { __builtin_amdgcn_s_sleep(1); \
;     if ((++_sp & 255u) == 0u) { if (xb_ld(&(bar)[XB_TMO])) break; if (_sp > XB_SPIN_CAP) { atomicAdd(&(bar)[XB_TMO], 1u); break; } } } } while (0)
; __device__ __forceinline__ void xcd_barrier(const XcdBarrier& b) {
;     ...
;             const unsigned og = xb_add(&bar[XB_TOP], 1u);
;             const unsigned tg = og / nx;
;             if (og + 1u == (tg + 1u) * nx) xb_add(&bar[XB_TOPGEN], 1u);
;             else XB_SPIN(xb_ld(&bar[XB_TOPGEN]) == tg, bar);
;             __builtin_amdgcn_fence(__ATOMIC_ACQUIRE, "agent");
;             xb_add(&bar[XB_XGEN(b.x)], 1u);
.LBB0_464:
	s_or_b64 exec, exec, s[10:11]
	s_and_saveexec_b64 s[10:11], s[14:15]
	s_cbranch_execz .LBB0_466
.LBB0_466:
	s_or_b64 exec, exec, s[10:11]
	s_waitcnt vmcnt(0)
	buffer_inv sc1
	s_waitcnt vmcnt(0)

; __device__ __forceinline__ unsigned xb_ld(unsigned* p)              { return __hip_atomic_load(p, __ATOMIC_RELAXED, __HIP_MEMORY_SCOPE_AGENT); }
; __device__ __forceinline__ unsigned xb_add(unsigned* p, unsigned v) { return __hip_atomic_fetch_add(p, v, __ATOMIC_RELAXED, __HIP_MEMORY_SCOPE_AGENT); }
; #define XB_SPIN(cond, bar) do { unsigned _sp = 0; while (cond) { __builtin_amdgcn_s_sleep(1); \
;     if ((++_sp & 255u) == 0u) { if (xb_ld(&(bar)[XB_TMO])) break; if (_sp > XB_SPIN_CAP) { atomicAdd(&(bar)[XB_TMO], 1u); break; } } } } while (0)
; __device__ __forceinline__ void xcd_barrier(const XcdBarrier& b) {
;     ...
;             const unsigned og = xb_add(&bar[XB_TOP], 1u);
;             const unsigned tg = og / nx;
;             if (og + 1u == (tg + 1u) * nx) xb_add(&bar[XB_TOPGEN], 1u);
;             else XB_SPIN(xb_ld(&bar[XB_TOPGEN]) == tg, bar);
;             __builtin_amdgcn_fence(__ATOMIC_ACQUIRE, "agent");
;             xb_add(&bar[XB_XGEN(b.x)], 1u);
.LBB0_545:
	s_or_b64 exec, exec, s[10:11]
	s_and_saveexec_b64 s[10:11], s[14:15]
	s_cbranch_execz .LBB0_547
.LBB0_547:
	s_or_b64 exec, exec, s[10:11]
	s_waitcnt vmcnt(0)
	buffer_inv sc1
	s_waitcnt vmcnt(0)

; __device__ __forceinline__ unsigned xb_ld(unsigned* p)              { return __hip_atomic_load(p, __ATOMIC_RELAXED, __HIP_MEMORY_SCOPE_AGENT); }
; __device__ __forceinline__ unsigned xb_add(unsigned* p, unsigned v) { return __hip_atomic_fetch_add(p, v, __ATOMIC_RELAXED, __HIP_MEMORY_SCOPE_AGENT); }
; #define XB_SPIN(cond, bar) do { unsigned _sp = 0; while (cond) { __builtin_amdgcn_s_sleep(1); \
;     if ((++_sp & 255u) == 0u) { if (xb_ld(&(bar)[XB_TMO])) break; if (_sp > XB_SPIN_CAP) { atomicAdd(&(bar)[XB_TMO], 1u); break; } } } } while (0)
; __device__ __forceinline__ void xcd_barrier(const XcdBarrier& b) {
;     ...
;             const unsigned og = xb_add(&bar[XB_TOP], 1u);
;             const unsigned tg = og / nx;
;             if (og + 1u == (tg + 1u) * nx) xb_add(&bar[XB_TOPGEN], 1u);
;             else XB_SPIN(xb_ld(&bar[XB_TOPGEN]) == tg, bar);
;             __builtin_amdgcn_fence(__ATOMIC_ACQUIRE, "agent");
;             xb_add(&bar[XB_XGEN(b.x)], 1u);
.LBB0_624:
	s_or_b64 exec, exec, s[10:11]
	s_and_saveexec_b64 s[10:11], s[14:15]
	s_cbranch_execz .LBB0_626
.LBB0_626:
	s_or_b64 exec, exec, s[10:11]
	s_waitcnt vmcnt(0)
	buffer_inv sc1
	s_waitcnt vmcnt(0)

; __device__ __forceinline__ unsigned xb_ld(unsigned* p)              { return __hip_atomic_load(p, __ATOMIC_RELAXED, __HIP_MEMORY_SCOPE_AGENT); }
; __device__ __forceinline__ unsigned xb_add(unsigned* p, unsigned v) { return __hip_atomic_fetch_add(p, v, __ATOMIC_RELAXED, __HIP_MEMORY_SCOPE_AGENT); }
; #define XB_SPIN(cond, bar) do { unsigned _sp = 0; while (cond) { __builtin_amdgcn_s_sleep(1); \
;     if ((++_sp & 255u) == 0u) { if (xb_ld(&(bar)[XB_TMO])) break; if (_sp > XB_SPIN_CAP) { atomicAdd(&(bar)[XB_TMO], 1u); break; } } } } while (0)
; __device__ __forceinline__ void xcd_barrier(const XcdBarrier& b) {
;     ...
;         const unsigned old = xb_add(&bar[XB_XSUB(b.x)], 1u);
;         const unsigned gen = old / nloc;
;         if (old + 1u == (gen + 1u) * nloc) {
;             __builtin_amdgcn_fence(__ATOMIC_RELEASE, "agent");
;             asm volatile("s_waitcnt vmcnt(0)" ::: "memory");
;             const unsigned og = xb_add(&bar[XB_TOP], 1u);
;             const unsigned tg = og / nx;
;             if (og + 1u == (tg + 1u) * nx) xb_add(&bar[XB_TOPGEN], 1u);
;             else XB_SPIN(xb_ld(&bar[XB_TOPGEN]) == tg, bar);
;             __builtin_amdgcn_fence(__ATOMIC_ACQUIRE, "agent");
;             xb_add(&bar[XB_XGEN(b.x)], 1u);
;             asm volatile("s_waitcnt vmcnt(0)" ::: "memory");
.LBB0_655:
	s_or_b64 exec, exec, s[10:11]
	v_cvt_f32_u32_e32 v4, v2
	s_waitcnt vmcnt(0)
	v_readfirstlane_b32 s3, v3
	v_sub_u32_e32 v3, 0, v2
	v_rcp_iflag_f32_e32 v4, v4
	v_add_u32_e32 v5, s3, v1
	v_mul_f32_e32 v4, 0x4f7ffffe, v4
	v_cvt_u32_f32_e32 v4, v4
	v_mul_lo_u32 v1, v3, v4
	v_mul_hi_u32 v1, v4, v1
	v_add_u32_e32 v1, v4, v1
	v_mul_hi_u32 v1, v5, v1
	v_mul_lo_u32 v3, v1, v2
	v_sub_u32_e32 v3, v5, v3
	v_add_u32_e32 v4, 1, v1
	v_cmp_ge_u32_e32 vcc, v3, v2
	s_nop 1
	v_cndmask_b32_e32 v1, v1, v4, vcc
	v_sub_u32_e32 v4, v3, v2
	v_cndmask_b32_e32 v3, v3, v4, vcc
	v_add_u32_e32 v4, 1, v1
	v_cmp_ge_u32_e32 vcc, v3, v2
	v_add_u32_e32 v3, 1, v5
	s_nop 0
	v_cndmask_b32_e32 v1, v1, v4, vcc
	v_mul_lo_u32 v4, v2, v1
	v_add_u32_e32 v2, v4, v2
	v_cmp_ne_u32_e32 vcc, v3, v2
	s_and_saveexec_b64 s[8:9], vcc
	s_xor_b64 s[8:9], exec, s[8:9]
	s_cbranch_execz .LBB0_669
	s_waitcnt lgkmcnt(0)
	v_mad_u32_u24 v3, v1, v0, v0
	v_mov_b32_e32 v0, 0x3400
	global_load_dword v0, v0, s[30:31] sc1
	s_add_u32 s12, s30, 0x3400
	s_addc_u32 s13, s31, 0
	s_waitcnt vmcnt(0)
	v_cmp_lt_u32_e32 vcc, v0, v3
	s_and_saveexec_b64 s[10:11], vcc
	s_cbranch_execz .LBB0_668
	s_mov_b32 s3, 1
	s_mov_b64 s[14:15], 0
	v_mov_b32_e32 v0, 0
	s_branch .LBB0_659

; __device__ __forceinline__ unsigned xb_ld(unsigned* p)              { return __hip_atomic_load(p, __ATOMIC_RELAXED, __HIP_MEMORY_SCOPE_AGENT); }
; #define XB_SPIN(cond, bar) do { unsigned _sp = 0; while (cond) { __builtin_amdgcn_s_sleep(1); \
;     if ((++_sp & 255u) == 0u) { if (xb_ld(&(bar)[XB_TMO])) break; if (_sp > XB_SPIN_CAP) { atomicAdd(&(bar)[XB_TMO], 1u); break; } } } } while (0)
; __device__ __forceinline__ void xcd_barrier(const XcdBarrier& b) {
;     ...
;             else XB_SPIN(xb_ld(&bar[XB_TOPGEN]) == tg, bar);
.LBB0_663:
	global_load_dword v2, v0, s[12:13] sc1
	s_add_i32 s3, s3, 1
	s_mov_b64 s[20:21], -1
	s_waitcnt vmcnt(0)
	v_cmp_ge_u32_e32 vcc, v2, v3
	s_orn2_b64 s[18:19], vcc, exec
	s_branch .LBB0_658

; __device__ __forceinline__ unsigned xb_ld(unsigned* p)              { return __hip_atomic_load(p, __ATOMIC_RELAXED, __HIP_MEMORY_SCOPE_AGENT); }
; __device__ __forceinline__ unsigned xb_add(unsigned* p, unsigned v) { return __hip_atomic_fetch_add(p, v, __ATOMIC_RELAXED, __HIP_MEMORY_SCOPE_AGENT); }
; #define XB_SPIN(cond, bar) do { unsigned _sp = 0; while (cond) { __builtin_amdgcn_s_sleep(1); \
;     if ((++_sp & 255u) == 0u) { if (xb_ld(&(bar)[XB_TMO])) break; if (_sp > XB_SPIN_CAP) { atomicAdd(&(bar)[XB_TMO], 1u); break; } } } } while (0)
; __device__ __forceinline__ void xcd_barrier(const XcdBarrier& b) {
;     ...
;         const unsigned old = xb_add(&bar[XB_XSUB(b.x)], 1u);
;         const unsigned gen = old / nloc;
;         if (old + 1u == (gen + 1u) * nloc) {
;             __builtin_amdgcn_fence(__ATOMIC_RELEASE, "agent");
;             asm volatile("s_waitcnt vmcnt(0)" ::: "memory");
;             const unsigned og = xb_add(&bar[XB_TOP], 1u);
;             const unsigned tg = og / nx;
;             if (og + 1u == (tg + 1u) * nx) xb_add(&bar[XB_TOPGEN], 1u);
;             else XB_SPIN(xb_ld(&bar[XB_TOPGEN]) == tg, bar);
;             __builtin_amdgcn_fence(__ATOMIC_ACQUIRE, "agent");
;             xb_add(&bar[XB_XGEN(b.x)], 1u);
;             asm volatile("s_waitcnt vmcnt(0)" ::: "memory");
.LBB0_672:
	s_or_b64 exec, exec, s[10:11]
	v_cvt_f32_u32_e32 v3, v0
	s_waitcnt vmcnt(0)
	v_readfirstlane_b32 s3, v2
	s_add_u32 s10, s30, 0x3400
	s_addc_u32 s11, s31, 0
	v_rcp_iflag_f32_e32 v3, v3
	v_add_u32_e32 v1, s3, v1
	v_add_u32_e32 v4, 1, v1
	s_mov_b64 s[12:13], -1
	v_mul_f32_e32 v2, 0x4f7ffffe, v3
	v_cvt_u32_f32_e32 v2, v2
	v_sub_u32_e32 v3, 0, v0
	v_mul_lo_u32 v3, v3, v2
	v_mul_hi_u32 v3, v2, v3
	v_add_u32_e32 v2, v2, v3
	v_mul_hi_u32 v2, v1, v2
	v_mul_lo_u32 v3, v2, v0
	v_sub_u32_e32 v1, v1, v3
	v_add_u32_e32 v5, 1, v2
	v_cmp_ge_u32_e32 vcc, v1, v0
	v_sub_u32_e32 v3, v1, v0
	s_nop 0
	v_cndmask_b32_e32 v2, v2, v5, vcc
	v_cndmask_b32_e32 v1, v1, v3, vcc
	v_add_u32_e32 v3, 1, v2
	v_cmp_ge_u32_e32 vcc, v1, v0
	s_nop 1
	v_cndmask_b32_e32 v2, v2, v3, vcc
	v_mul_lo_u32 v1, v0, v2
	v_add_u32_e32 v0, v1, v0
	v_mov_b32_e32 v6, v0
	v_cmp_ne_u32_e32 vcc, v4, v0
	v_mov_b64_e32 v[0:1], s[10:11]
	s_and_saveexec_b64 s[8:9], vcc
	s_cbranch_execz .LBB0_684
	v_mov_b32_e32 v0, 0
	global_load_dword v1, v0, s[10:11] sc1
	s_mov_b64 s[16:17], 0
	s_waitcnt vmcnt(0)
	v_cmp_lt_u32_e32 vcc, v1, v6
	s_and_saveexec_b64 s[14:15], vcc
	s_cbranch_execz .LBB0_683
	s_add_u32 s12, s30, 0x200
	s_addc_u32 s13, s31, 0
	s_mov_b32 s3, 1
	s_branch .LBB0_676

; __device__ __forceinline__ unsigned xb_ld(unsigned* p)              { return __hip_atomic_load(p, __ATOMIC_RELAXED, __HIP_MEMORY_SCOPE_AGENT); }
; #define XB_SPIN(cond, bar) do { unsigned _sp = 0; while (cond) { __builtin_amdgcn_s_sleep(1); \
;     if ((++_sp & 255u) == 0u) { if (xb_ld(&(bar)[XB_TMO])) break; if (_sp > XB_SPIN_CAP) { atomicAdd(&(bar)[XB_TMO], 1u); break; } } } } while (0)
; __device__ __forceinline__ void xcd_barrier(const XcdBarrier& b) {
;     ...
;             else XB_SPIN(xb_ld(&bar[XB_TOPGEN]) == tg, bar);
.LBB0_680:
	global_load_dword v1, v0, s[10:11] sc1
	s_add_i32 s3, s3, 1
	s_mov_b64 s[20:21], -1
	s_waitcnt vmcnt(0)
	v_cmp_ge_u32_e32 vcc, v1, v6
	s_orn2_b64 s[24:25], vcc, exec
	s_branch .LBB0_675

; __device__ __forceinline__ unsigned xb_ld(unsigned* p)              { return __hip_atomic_load(p, __ATOMIC_RELAXED, __HIP_MEMORY_SCOPE_AGENT); }
; __device__ __forceinline__ unsigned xb_add(unsigned* p, unsigned v) { return __hip_atomic_fetch_add(p, v, __ATOMIC_RELAXED, __HIP_MEMORY_SCOPE_AGENT); }
; #define XB_SPIN(cond, bar) do { unsigned _sp = 0; while (cond) { __builtin_amdgcn_s_sleep(1); \
;     if ((++_sp & 255u) == 0u) { if (xb_ld(&(bar)[XB_TMO])) break; if (_sp > XB_SPIN_CAP) { atomicAdd(&(bar)[XB_TMO], 1u); break; } } } } while (0)
; __device__ __forceinline__ void xcd_barrier(const XcdBarrier& b) {
;     ...
;             const unsigned og = xb_add(&bar[XB_TOP], 1u);
;             const unsigned tg = og / nx;
;             if (og + 1u == (tg + 1u) * nx) xb_add(&bar[XB_TOPGEN], 1u);
;             else XB_SPIN(xb_ld(&bar[XB_TOPGEN]) == tg, bar);
;             __builtin_amdgcn_fence(__ATOMIC_ACQUIRE, "agent");
;             xb_add(&bar[XB_XGEN(b.x)], 1u);
.LBB0_684:
	s_or_b64 exec, exec, s[8:9]
	s_and_saveexec_b64 s[8:9], s[12:13]
	s_cbranch_execz .LBB0_686
.LBB0_686:
	s_or_b64 exec, exec, s[8:9]
	s_waitcnt vmcnt(0)
	buffer_inv sc1
	s_waitcnt vmcnt(0)

; __device__ __forceinline__ unsigned xb_ld(unsigned* p)              { return __hip_atomic_load(p, __ATOMIC_RELAXED, __HIP_MEMORY_SCOPE_AGENT); }
; __device__ __forceinline__ unsigned xb_add(unsigned* p, unsigned v) { return __hip_atomic_fetch_add(p, v, __ATOMIC_RELAXED, __HIP_MEMORY_SCOPE_AGENT); }
; #define XB_SPIN(cond, bar) do { unsigned _sp = 0; while (cond) { __builtin_amdgcn_s_sleep(1); \
;     if ((++_sp & 255u) == 0u) { if (xb_ld(&(bar)[XB_TMO])) break; if (_sp > XB_SPIN_CAP) { atomicAdd(&(bar)[XB_TMO], 1u); break; } } } } while (0)
; __device__ __forceinline__ void xcd_barrier(const XcdBarrier& b) {
;     ...
;             const unsigned og = xb_add(&bar[XB_TOP], 1u);
;             const unsigned tg = og / nx;
;             if (og + 1u == (tg + 1u) * nx) xb_add(&bar[XB_TOPGEN], 1u);
;             else XB_SPIN(xb_ld(&bar[XB_TOPGEN]) == tg, bar);
;             __builtin_amdgcn_fence(__ATOMIC_ACQUIRE, "agent");
;             xb_add(&bar[XB_XGEN(b.x)], 1u);
.LBB0_779:
	s_or_b64 exec, exec, s[10:11]
	s_and_saveexec_b64 s[10:11], s[14:15]
	s_cbranch_execz .LBB0_781
.LBB0_781:
	s_or_b64 exec, exec, s[10:11]
	s_waitcnt vmcnt(0)
	buffer_inv sc1
	s_waitcnt vmcnt(0)

; __device__ __forceinline__ unsigned xb_ld(unsigned* p)              { return __hip_atomic_load(p, __ATOMIC_RELAXED, __HIP_MEMORY_SCOPE_AGENT); }
; __device__ __forceinline__ unsigned xb_add(unsigned* p, unsigned v) { return __hip_atomic_fetch_add(p, v, __ATOMIC_RELAXED, __HIP_MEMORY_SCOPE_AGENT); }
; #define XB_SPIN(cond, bar) do { unsigned _sp = 0; while (cond) { __builtin_amdgcn_s_sleep(1); \
;     if ((++_sp & 255u) == 0u) { if (xb_ld(&(bar)[XB_TMO])) break; if (_sp > XB_SPIN_CAP) { atomicAdd(&(bar)[XB_TMO], 1u); break; } } } } while (0)
; __device__ __forceinline__ void xcd_barrier(const XcdBarrier& b) {
;     ...
;             const unsigned og = xb_add(&bar[XB_TOP], 1u);
;             const unsigned tg = og / nx;
;             if (og + 1u == (tg + 1u) * nx) xb_add(&bar[XB_TOPGEN], 1u);
;             else XB_SPIN(xb_ld(&bar[XB_TOPGEN]) == tg, bar);
;             __builtin_amdgcn_fence(__ATOMIC_ACQUIRE, "agent");
;             xb_add(&bar[XB_XGEN(b.x)], 1u);
.LBB0_864:
	s_or_b64 exec, exec, s[10:11]
	s_and_saveexec_b64 s[10:11], s[14:15]
	s_cbranch_execz .LBB0_866
.LBB0_866:
	s_or_b64 exec, exec, s[10:11]
	s_waitcnt vmcnt(0)
	buffer_inv sc1
	s_waitcnt vmcnt(0)

; __device__ __forceinline__ unsigned xb_ld(unsigned* p)              { return __hip_atomic_load(p, __ATOMIC_RELAXED, __HIP_MEMORY_SCOPE_AGENT); }
; __device__ __forceinline__ unsigned xb_add(unsigned* p, unsigned v) { return __hip_atomic_fetch_add(p, v, __ATOMIC_RELAXED, __HIP_MEMORY_SCOPE_AGENT); }
; #define XB_SPIN(cond, bar) do { unsigned _sp = 0; while (cond) { __builtin_amdgcn_s_sleep(1); \
;     if ((++_sp & 255u) == 0u) { if (xb_ld(&(bar)[XB_TMO])) break; if (_sp > XB_SPIN_CAP) { atomicAdd(&(bar)[XB_TMO], 1u); break; } } } } while (0)
; __device__ __forceinline__ void xcd_barrier(const XcdBarrier& b) {
;     ...
;             const unsigned og = xb_add(&bar[XB_TOP], 1u);
;             const unsigned tg = og / nx;
;             if (og + 1u == (tg + 1u) * nx) xb_add(&bar[XB_TOPGEN], 1u);
;             else XB_SPIN(xb_ld(&bar[XB_TOPGEN]) == tg, bar);
;             __builtin_amdgcn_fence(__ATOMIC_ACQUIRE, "agent");
;             xb_add(&bar[XB_XGEN(b.x)], 1u);
.LBB0_924:
	s_or_b64 exec, exec, s[10:11]
	s_and_saveexec_b64 s[10:11], s[14:15]
	s_cbranch_execz .LBB0_926
.LBB0_926:
	s_or_b64 exec, exec, s[10:11]
	s_waitcnt vmcnt(0)
	buffer_inv sc1
	s_waitcnt vmcnt(0)

; __device__ __forceinline__ unsigned xb_ld(unsigned* p)              { return __hip_atomic_load(p, __ATOMIC_RELAXED, __HIP_MEMORY_SCOPE_AGENT); }
; __device__ __forceinline__ unsigned xb_add(unsigned* p, unsigned v) { return __hip_atomic_fetch_add(p, v, __ATOMIC_RELAXED, __HIP_MEMORY_SCOPE_AGENT); }
; #define XB_SPIN(cond, bar) do { unsigned _sp = 0; while (cond) { __builtin_amdgcn_s_sleep(1); \
;     if ((++_sp & 255u) == 0u) { if (xb_ld(&(bar)[XB_TMO])) break; if (_sp > XB_SPIN_CAP) { atomicAdd(&(bar)[XB_TMO], 1u); break; } } } } while (0)
; __device__ __forceinline__ void xcd_barrier(const XcdBarrier& b) {
;     ...
;             const unsigned og = xb_add(&bar[XB_TOP], 1u);
;             const unsigned tg = og / nx;
;             if (og + 1u == (tg + 1u) * nx) xb_add(&bar[XB_TOPGEN], 1u);
;             else XB_SPIN(xb_ld(&bar[XB_TOPGEN]) == tg, bar);
;             __builtin_amdgcn_fence(__ATOMIC_ACQUIRE, "agent");
;             xb_add(&bar[XB_XGEN(b.x)], 1u);
.LBB0_1089:
	s_or_b64 exec, exec, s[10:11]
	s_and_saveexec_b64 s[10:11], s[14:15]
	s_cbranch_execz .LBB0_1091
.LBB0_1091:
	s_or_b64 exec, exec, s[10:11]
	s_waitcnt vmcnt(0)
	buffer_inv sc1
	s_waitcnt vmcnt(0)

; __device__ __forceinline__ unsigned xb_ld(unsigned* p)              { return __hip_atomic_load(p, __ATOMIC_RELAXED, __HIP_MEMORY_SCOPE_AGENT); }
; __device__ __forceinline__ unsigned xb_add(unsigned* p, unsigned v) { return __hip_atomic_fetch_add(p, v, __ATOMIC_RELAXED, __HIP_MEMORY_SCOPE_AGENT); }
; #define XB_SPIN(cond, bar) do { unsigned _sp = 0; while (cond) { __builtin_amdgcn_s_sleep(1); \
;     if ((++_sp & 255u) == 0u) { if (xb_ld(&(bar)[XB_TMO])) break; if (_sp > XB_SPIN_CAP) { atomicAdd(&(bar)[XB_TMO], 1u); break; } } } } while (0)
; __device__ __forceinline__ void xcd_barrier(const XcdBarrier& b) {
;     ...
;             const unsigned og = xb_add(&bar[XB_TOP], 1u);
;             const unsigned tg = og / nx;
;             if (og + 1u == (tg + 1u) * nx) xb_add(&bar[XB_TOPGEN], 1u);
;             else XB_SPIN(xb_ld(&bar[XB_TOPGEN]) == tg, bar);
;             __builtin_amdgcn_fence(__ATOMIC_ACQUIRE, "agent");
;             xb_add(&bar[XB_XGEN(b.x)], 1u);
.LBB0_1200:
	s_or_b64 exec, exec, s[10:11]
	s_and_saveexec_b64 s[10:11], s[14:15]
	s_cbranch_execz .LBB0_1202
.LBB0_1202:
	s_or_b64 exec, exec, s[10:11]
	s_waitcnt vmcnt(0)
	buffer_inv sc1
	s_waitcnt vmcnt(0)

; __device__ __forceinline__ unsigned xb_ld(unsigned* p)              { return __hip_atomic_load(p, __ATOMIC_RELAXED, __HIP_MEMORY_SCOPE_AGENT); }
; __device__ __forceinline__ unsigned xb_add(unsigned* p, unsigned v) { return __hip_atomic_fetch_add(p, v, __ATOMIC_RELAXED, __HIP_MEMORY_SCOPE_AGENT); }
; #define XB_SPIN(cond, bar) do { unsigned _sp = 0; while (cond) { __builtin_amdgcn_s_sleep(1); \
;     if ((++_sp & 255u) == 0u) { if (xb_ld(&(bar)[XB_TMO])) break; if (_sp > XB_SPIN_CAP) { atomicAdd(&(bar)[XB_TMO], 1u); break; } } } } while (0)
; __device__ __forceinline__ void xcd_barrier(const XcdBarrier& b) {
;     ...
;             const unsigned og = xb_add(&bar[XB_TOP], 1u);
;             const unsigned tg = og / nx;
;             if (og + 1u == (tg + 1u) * nx) xb_add(&bar[XB_TOPGEN], 1u);
;             else XB_SPIN(xb_ld(&bar[XB_TOPGEN]) == tg, bar);
;             __builtin_amdgcn_fence(__ATOMIC_ACQUIRE, "agent");
;             xb_add(&bar[XB_XGEN(b.x)], 1u);
.LBB0_1281:
	s_or_b64 exec, exec, s[10:11]
	s_and_saveexec_b64 s[10:11], s[14:15]
	s_cbranch_execz .LBB0_1283
.LBB0_1283:
	s_or_b64 exec, exec, s[10:11]
	s_waitcnt vmcnt(0)
	buffer_inv sc1
	s_waitcnt vmcnt(0)

; __device__ __forceinline__ unsigned xb_ld(unsigned* p)              { return __hip_atomic_load(p, __ATOMIC_RELAXED, __HIP_MEMORY_SCOPE_AGENT); }
; __device__ __forceinline__ unsigned xb_add(unsigned* p, unsigned v) { return __hip_atomic_fetch_add(p, v, __ATOMIC_RELAXED, __HIP_MEMORY_SCOPE_AGENT); }
; #define XB_SPIN(cond, bar) do { unsigned _sp = 0; while (cond) { __builtin_amdgcn_s_sleep(1); \
;     if ((++_sp & 255u) == 0u) { if (xb_ld(&(bar)[XB_TMO])) break; if (_sp > XB_SPIN_CAP) { atomicAdd(&(bar)[XB_TMO], 1u); break; } } } } while (0)
; __device__ __forceinline__ void xcd_barrier(const XcdBarrier& b) {
;     ...
;             const unsigned og = xb_add(&bar[XB_TOP], 1u);
;             const unsigned tg = og / nx;
;             if (og + 1u == (tg + 1u) * nx) xb_add(&bar[XB_TOPGEN], 1u);
;             else XB_SPIN(xb_ld(&bar[XB_TOPGEN]) == tg, bar);
;             __builtin_amdgcn_fence(__ATOMIC_ACQUIRE, "agent");
;             xb_add(&bar[XB_XGEN(b.x)], 1u);
.LBB0_1360:
	s_or_b64 exec, exec, s[10:11]
	s_and_saveexec_b64 s[10:11], s[14:15]
	s_cbranch_execz .LBB0_1362
.LBB0_1362:
	s_or_b64 exec, exec, s[10:11]
	s_waitcnt vmcnt(0)
	buffer_inv sc1
	s_waitcnt vmcnt(0)

; __device__ __forceinline__ unsigned xb_ld(unsigned* p)              { return __hip_atomic_load(p, __ATOMIC_RELAXED, __HIP_MEMORY_SCOPE_AGENT); }
; __device__ __forceinline__ unsigned xb_add(unsigned* p, unsigned v) { return __hip_atomic_fetch_add(p, v, __ATOMIC_RELAXED, __HIP_MEMORY_SCOPE_AGENT); }
; #define XB_SPIN(cond, bar) do { unsigned _sp = 0; while (cond) { __builtin_amdgcn_s_sleep(1); \
;     if ((++_sp & 255u) == 0u) { if (xb_ld(&(bar)[XB_TMO])) break; if (_sp > XB_SPIN_CAP) { atomicAdd(&(bar)[XB_TMO], 1u); break; } } } } while (0)
; __device__ __forceinline__ void xcd_barrier(const XcdBarrier& b) {
;     ...
;             const unsigned og = xb_add(&bar[XB_TOP], 1u);
;             const unsigned tg = og / nx;
;             if (og + 1u == (tg + 1u) * nx) xb_add(&bar[XB_TOPGEN], 1u);
;             else XB_SPIN(xb_ld(&bar[XB_TOPGEN]) == tg, bar);
;             __builtin_amdgcn_fence(__ATOMIC_ACQUIRE, "agent");
;             xb_add(&bar[XB_XGEN(b.x)], 1u);
.LBB0_1432:
	s_or_b64 exec, exec, s[10:11]
	s_and_saveexec_b64 s[10:11], s[14:15]
	s_cbranch_execz .LBB0_1434
.LBB0_1434:
	s_or_b64 exec, exec, s[10:11]
	s_waitcnt vmcnt(0)
	buffer_inv sc1
	s_waitcnt vmcnt(0)

; __device__ __forceinline__ unsigned xb_ld(unsigned* p)              { return __hip_atomic_load(p, __ATOMIC_RELAXED, __HIP_MEMORY_SCOPE_AGENT); }
; __device__ __forceinline__ unsigned xb_add(unsigned* p, unsigned v) { return __hip_atomic_fetch_add(p, v, __ATOMIC_RELAXED, __HIP_MEMORY_SCOPE_AGENT); }
; #define XB_SPIN(cond, bar) do { unsigned _sp = 0; while (cond) { __builtin_amdgcn_s_sleep(1); \
;     if ((++_sp & 255u) == 0u) { if (xb_ld(&(bar)[XB_TMO])) break; if (_sp > XB_SPIN_CAP) { atomicAdd(&(bar)[XB_TMO], 1u); break; } } } } while (0)
; __device__ __forceinline__ void xcd_barrier(const XcdBarrier& b) {
;     ...
;             const unsigned og = xb_add(&bar[XB_TOP], 1u);
;             const unsigned tg = og / nx;
;             if (og + 1u == (tg + 1u) * nx) xb_add(&bar[XB_TOPGEN], 1u);
;             else XB_SPIN(xb_ld(&bar[XB_TOPGEN]) == tg, bar);
;             __builtin_amdgcn_fence(__ATOMIC_ACQUIRE, "agent");
;             xb_add(&bar[XB_XGEN(b.x)], 1u);
.LBB0_1588:
	s_or_b64 exec, exec, s[10:11]
	s_and_saveexec_b64 s[10:11], s[14:15]
	s_cbranch_execz .LBB0_1590
.LBB0_1590:
	s_or_b64 exec, exec, s[10:11]
	s_waitcnt vmcnt(0)
	buffer_inv sc1
	s_waitcnt vmcnt(0)

; __device__ __forceinline__ unsigned xb_ld(unsigned* p)              { return __hip_atomic_load(p, __ATOMIC_RELAXED, __HIP_MEMORY_SCOPE_AGENT); }
; __device__ __forceinline__ unsigned xb_add(unsigned* p, unsigned v) { return __hip_atomic_fetch_add(p, v, __ATOMIC_RELAXED, __HIP_MEMORY_SCOPE_AGENT); }
; #define XB_SPIN(cond, bar) do { unsigned _sp = 0; while (cond) { __builtin_amdgcn_s_sleep(1); \
;     if ((++_sp & 255u) == 0u) { if (xb_ld(&(bar)[XB_TMO])) break; if (_sp > XB_SPIN_CAP) { atomicAdd(&(bar)[XB_TMO], 1u); break; } } } } while (0)
; __device__ __forceinline__ void xcd_barrier(const XcdBarrier& b) {
;     ...
;             const unsigned og = xb_add(&bar[XB_TOP], 1u);
;             const unsigned tg = og / nx;
;             if (og + 1u == (tg + 1u) * nx) xb_add(&bar[XB_TOPGEN], 1u);
;             else XB_SPIN(xb_ld(&bar[XB_TOPGEN]) == tg, bar);
;             __builtin_amdgcn_fence(__ATOMIC_ACQUIRE, "agent");
;             xb_add(&bar[XB_XGEN(b.x)], 1u);
.LBB0_1663:
	s_or_b64 exec, exec, s[10:11]
	s_and_saveexec_b64 s[10:11], s[14:15]
	s_cbranch_execz .LBB0_1665
.LBB0_1665:
	s_or_b64 exec, exec, s[10:11]
	s_waitcnt vmcnt(0)
	buffer_inv sc1
	s_waitcnt vmcnt(0)

; __device__ __forceinline__ unsigned xb_ld(unsigned* p)              { return __hip_atomic_load(p, __ATOMIC_RELAXED, __HIP_MEMORY_SCOPE_AGENT); }
; __device__ __forceinline__ unsigned xb_add(unsigned* p, unsigned v) { return __hip_atomic_fetch_add(p, v, __ATOMIC_RELAXED, __HIP_MEMORY_SCOPE_AGENT); }
; #define XB_SPIN(cond, bar) do { unsigned _sp = 0; while (cond) { __builtin_amdgcn_s_sleep(1); \
;     if ((++_sp & 255u) == 0u) { if (xb_ld(&(bar)[XB_TMO])) break; if (_sp > XB_SPIN_CAP) { atomicAdd(&(bar)[XB_TMO], 1u); break; } } } } while (0)
; __device__ __forceinline__ void xcd_barrier(const XcdBarrier& b) {
;     ...
;         const unsigned old = xb_add(&bar[XB_XSUB(b.x)], 1u);
;         const unsigned gen = old / nloc;
;         if (old + 1u == (gen + 1u) * nloc) {
;             __builtin_amdgcn_fence(__ATOMIC_RELEASE, "agent");
;             asm volatile("s_waitcnt vmcnt(0)" ::: "memory");
;             const unsigned og = xb_add(&bar[XB_TOP], 1u);
;             const unsigned tg = og / nx;
;             if (og + 1u == (tg + 1u) * nx) xb_add(&bar[XB_TOPGEN], 1u);
;             else XB_SPIN(xb_ld(&bar[XB_TOPGEN]) == tg, bar);
;             __builtin_amdgcn_fence(__ATOMIC_ACQUIRE, "agent");
;             xb_add(&bar[XB_XGEN(b.x)], 1u);
;             asm volatile("s_waitcnt vmcnt(0)" ::: "memory");
.LBB0_1736:
	s_or_b64 exec, exec, s[10:11]
	v_cvt_f32_u32_e32 v4, v2
	s_waitcnt vmcnt(0)
	v_readfirstlane_b32 s8, v3
	v_sub_u32_e32 v3, 0, v2
	v_rcp_iflag_f32_e32 v4, v4
	v_add_u32_e32 v5, s8, v1
	v_mul_f32_e32 v4, 0x4f7ffffe, v4
	v_cvt_u32_f32_e32 v4, v4
	v_mul_lo_u32 v1, v3, v4
	v_mul_hi_u32 v1, v4, v1
	v_add_u32_e32 v1, v4, v1
	v_mul_hi_u32 v1, v5, v1
	v_mul_lo_u32 v3, v1, v2
	v_sub_u32_e32 v3, v5, v3
	v_add_u32_e32 v4, 1, v1
	v_cmp_ge_u32_e32 vcc, v3, v2
	s_nop 1
	v_cndmask_b32_e32 v1, v1, v4, vcc
	v_sub_u32_e32 v4, v3, v2
	v_cndmask_b32_e32 v3, v3, v4, vcc
	v_add_u32_e32 v4, 1, v1
	v_cmp_ge_u32_e32 vcc, v3, v2
	v_add_u32_e32 v3, 1, v5
	s_nop 0
	v_cndmask_b32_e32 v1, v1, v4, vcc
	v_mul_lo_u32 v4, v2, v1
	v_add_u32_e32 v2, v4, v2
	v_cmp_ne_u32_e32 vcc, v3, v2
	s_and_saveexec_b64 s[8:9], vcc
	s_xor_b64 s[8:9], exec, s[8:9]
	s_cbranch_execz .LBB0_1750
	s_waitcnt lgkmcnt(0)
	v_mad_u32_u24 v3, v1, v0, v0
	v_mov_b32_e32 v0, 0x3400
	global_load_dword v0, v0, s[30:31] sc1
	s_add_u32 s12, s30, 0x3400
	s_addc_u32 s13, s31, 0
	s_waitcnt vmcnt(0)
	v_cmp_lt_u32_e32 vcc, v0, v3
	s_and_saveexec_b64 s[10:11], vcc
	s_cbranch_execz .LBB0_1749
	s_mov_b32 s24, 1
	s_mov_b64 s[14:15], 0
	v_mov_b32_e32 v0, 0
	s_branch .LBB0_1740

; __device__ __forceinline__ unsigned xb_ld(unsigned* p)              { return __hip_atomic_load(p, __ATOMIC_RELAXED, __HIP_MEMORY_SCOPE_AGENT); }
; #define XB_SPIN(cond, bar) do { unsigned _sp = 0; while (cond) { __builtin_amdgcn_s_sleep(1); \
;     if ((++_sp & 255u) == 0u) { if (xb_ld(&(bar)[XB_TMO])) break; if (_sp > XB_SPIN_CAP) { atomicAdd(&(bar)[XB_TMO], 1u); break; } } } } while (0)
; __device__ __forceinline__ void xcd_barrier(const XcdBarrier& b) {
;     ...
;             else XB_SPIN(xb_ld(&bar[XB_TOPGEN]) == tg, bar);
.LBB0_1744:
	global_load_dword v2, v0, s[12:13] sc1
	s_add_i32 s24, s24, 1
	s_mov_b64 s[20:21], -1
	s_waitcnt vmcnt(0)
	v_cmp_ge_u32_e32 vcc, v2, v3
	s_orn2_b64 s[18:19], vcc, exec
	s_branch .LBB0_1739

; __device__ __forceinline__ unsigned xb_ld(unsigned* p)              { return __hip_atomic_load(p, __ATOMIC_RELAXED, __HIP_MEMORY_SCOPE_AGENT); }
; __device__ __forceinline__ unsigned xb_add(unsigned* p, unsigned v) { return __hip_atomic_fetch_add(p, v, __ATOMIC_RELAXED, __HIP_MEMORY_SCOPE_AGENT); }
; #define XB_SPIN(cond, bar) do { unsigned _sp = 0; while (cond) { __builtin_amdgcn_s_sleep(1); \
;     if ((++_sp & 255u) == 0u) { if (xb_ld(&(bar)[XB_TMO])) break; if (_sp > XB_SPIN_CAP) { atomicAdd(&(bar)[XB_TMO], 1u); break; } } } } while (0)
; __device__ __forceinline__ void xcd_barrier(const XcdBarrier& b) {
;     ...
;         const unsigned old = xb_add(&bar[XB_XSUB(b.x)], 1u);
;         const unsigned gen = old / nloc;
;         if (old + 1u == (gen + 1u) * nloc) {
;             __builtin_amdgcn_fence(__ATOMIC_RELEASE, "agent");
;             asm volatile("s_waitcnt vmcnt(0)" ::: "memory");
;             const unsigned og = xb_add(&bar[XB_TOP], 1u);
;             const unsigned tg = og / nx;
;             if (og + 1u == (tg + 1u) * nx) xb_add(&bar[XB_TOPGEN], 1u);
;             else XB_SPIN(xb_ld(&bar[XB_TOPGEN]) == tg, bar);
;             __builtin_amdgcn_fence(__ATOMIC_ACQUIRE, "agent");
;             xb_add(&bar[XB_XGEN(b.x)], 1u);
;             asm volatile("s_waitcnt vmcnt(0)" ::: "memory");
.LBB0_1753:
	s_or_b64 exec, exec, s[10:11]
	v_cvt_f32_u32_e32 v3, v0
	s_waitcnt vmcnt(0)
	v_readfirstlane_b32 s8, v2
	s_add_u32 s10, s30, 0x3400
	s_addc_u32 s11, s31, 0
	v_rcp_iflag_f32_e32 v3, v3
	v_add_u32_e32 v1, s8, v1
	v_add_u32_e32 v4, 1, v1
	s_mov_b64 s[12:13], -1
	v_mul_f32_e32 v2, 0x4f7ffffe, v3
	v_cvt_u32_f32_e32 v2, v2
	v_sub_u32_e32 v3, 0, v0
	v_mul_lo_u32 v3, v3, v2
	v_mul_hi_u32 v3, v2, v3
	v_add_u32_e32 v2, v2, v3
	v_mul_hi_u32 v2, v1, v2
	v_mul_lo_u32 v3, v2, v0
	v_sub_u32_e32 v1, v1, v3
	v_add_u32_e32 v5, 1, v2
	v_cmp_ge_u32_e32 vcc, v1, v0
	v_sub_u32_e32 v3, v1, v0
	s_nop 0
	v_cndmask_b32_e32 v2, v2, v5, vcc
	v_cndmask_b32_e32 v1, v1, v3, vcc
	v_add_u32_e32 v3, 1, v2
	v_cmp_ge_u32_e32 vcc, v1, v0
	s_nop 1
	v_cndmask_b32_e32 v2, v2, v3, vcc
	v_mul_lo_u32 v1, v0, v2
	v_add_u32_e32 v0, v1, v0
	v_mov_b32_e32 v6, v0
	v_cmp_ne_u32_e32 vcc, v4, v0
	v_mov_b64_e32 v[0:1], s[10:11]
	s_and_saveexec_b64 s[8:9], vcc
	s_cbranch_execz .LBB0_1765
	v_mov_b32_e32 v0, 0
	global_load_dword v1, v0, s[10:11] sc1
	s_mov_b64 s[16:17], 0
	s_waitcnt vmcnt(0)
	v_cmp_lt_u32_e32 vcc, v1, v6
	s_and_saveexec_b64 s[14:15], vcc
	s_cbranch_execz .LBB0_1764
	s_add_u32 s12, s30, 0x200
	s_addc_u32 s13, s31, 0
	s_mov_b32 s26, 1
	s_branch .LBB0_1757

; __device__ __forceinline__ unsigned xb_ld(unsigned* p)              { return __hip_atomic_load(p, __ATOMIC_RELAXED, __HIP_MEMORY_SCOPE_AGENT); }
; #define XB_SPIN(cond, bar) do { unsigned _sp = 0; while (cond) { __builtin_amdgcn_s_sleep(1); \
;     if ((++_sp & 255u) == 0u) { if (xb_ld(&(bar)[XB_TMO])) break; if (_sp > XB_SPIN_CAP) { atomicAdd(&(bar)[XB_TMO], 1u); break; } } } } while (0)
; __device__ __forceinline__ void xcd_barrier(const XcdBarrier& b) {
;     ...
;             else XB_SPIN(xb_ld(&bar[XB_TOPGEN]) == tg, bar);
.LBB0_1761:
	global_load_dword v1, v0, s[10:11] sc1
	s_add_i32 s26, s26, 1
	s_mov_b64 s[20:21], -1
	s_waitcnt vmcnt(0)
	v_cmp_ge_u32_e32 vcc, v1, v6
	s_orn2_b64 s[24:25], vcc, exec
	s_branch .LBB0_1756

; __device__ __forceinline__ unsigned xb_ld(unsigned* p)              { return __hip_atomic_load(p, __ATOMIC_RELAXED, __HIP_MEMORY_SCOPE_AGENT); }
; __device__ __forceinline__ unsigned xb_add(unsigned* p, unsigned v) { return __hip_atomic_fetch_add(p, v, __ATOMIC_RELAXED, __HIP_MEMORY_SCOPE_AGENT); }
; #define XB_SPIN(cond, bar) do { unsigned _sp = 0; while (cond) { __builtin_amdgcn_s_sleep(1); \
;     if ((++_sp & 255u) == 0u) { if (xb_ld(&(bar)[XB_TMO])) break; if (_sp > XB_SPIN_CAP) { atomicAdd(&(bar)[XB_TMO], 1u); break; } } } } while (0)
; __device__ __forceinline__ void xcd_barrier(const XcdBarrier& b) {
;     ...
;             const unsigned og = xb_add(&bar[XB_TOP], 1u);
;             const unsigned tg = og / nx;
;             if (og + 1u == (tg + 1u) * nx) xb_add(&bar[XB_TOPGEN], 1u);
;             else XB_SPIN(xb_ld(&bar[XB_TOPGEN]) == tg, bar);
;             __builtin_amdgcn_fence(__ATOMIC_ACQUIRE, "agent");
;             xb_add(&bar[XB_XGEN(b.x)], 1u);
.LBB0_1765:
	s_or_b64 exec, exec, s[8:9]
	s_and_saveexec_b64 s[8:9], s[12:13]
	s_cbranch_execz .LBB0_1767
.LBB0_1767:
	s_or_b64 exec, exec, s[8:9]
	s_waitcnt vmcnt(0)
	buffer_inv sc1
	s_waitcnt vmcnt(0)

; __device__ __forceinline__ unsigned xb_ld(unsigned* p)              { return __hip_atomic_load(p, __ATOMIC_RELAXED, __HIP_MEMORY_SCOPE_AGENT); }
; __device__ __forceinline__ unsigned xb_add(unsigned* p, unsigned v) { return __hip_atomic_fetch_add(p, v, __ATOMIC_RELAXED, __HIP_MEMORY_SCOPE_AGENT); }
; #define XB_SPIN(cond, bar) do { unsigned _sp = 0; while (cond) { __builtin_amdgcn_s_sleep(1); \
;     if ((++_sp & 255u) == 0u) { if (xb_ld(&(bar)[XB_TMO])) break; if (_sp > XB_SPIN_CAP) { atomicAdd(&(bar)[XB_TMO], 1u); break; } } } } while (0)
; __device__ __forceinline__ void xcd_barrier(const XcdBarrier& b) {
;     ...
;         const unsigned old = xb_add(&bar[XB_XSUB(b.x)], 1u);
;         const unsigned gen = old / nloc;
;         if (old + 1u == (gen + 1u) * nloc) {
;             __builtin_amdgcn_fence(__ATOMIC_RELEASE, "agent");
;             asm volatile("s_waitcnt vmcnt(0)" ::: "memory");
;             const unsigned og = xb_add(&bar[XB_TOP], 1u);
;             const unsigned tg = og / nx;
;             if (og + 1u == (tg + 1u) * nx) xb_add(&bar[XB_TOPGEN], 1u);
;             else XB_SPIN(xb_ld(&bar[XB_TOPGEN]) == tg, bar);
;             __builtin_amdgcn_fence(__ATOMIC_ACQUIRE, "agent");
;             xb_add(&bar[XB_XGEN(b.x)], 1u);
;             asm volatile("s_waitcnt vmcnt(0)" ::: "memory");
.LBB0_1796:
	s_or_b64 exec, exec, s[6:7]
	v_cvt_f32_u32_e32 v4, v2
	s_waitcnt vmcnt(0)
	v_readfirstlane_b32 s4, v3
	v_sub_u32_e32 v3, 0, v2
	v_rcp_iflag_f32_e32 v4, v4
	v_add_u32_e32 v5, s4, v1
	v_mul_f32_e32 v4, 0x4f7ffffe, v4
	v_cvt_u32_f32_e32 v4, v4
	v_mul_lo_u32 v1, v3, v4
	v_mul_hi_u32 v1, v4, v1
	v_add_u32_e32 v1, v4, v1
	v_mul_hi_u32 v1, v5, v1
	v_mul_lo_u32 v3, v1, v2
	v_sub_u32_e32 v3, v5, v3
	v_add_u32_e32 v4, 1, v1
	v_cmp_ge_u32_e32 vcc, v3, v2
	s_nop 1
	v_cndmask_b32_e32 v1, v1, v4, vcc
	v_sub_u32_e32 v4, v3, v2
	v_cndmask_b32_e32 v3, v3, v4, vcc
	v_add_u32_e32 v4, 1, v1
	v_cmp_ge_u32_e32 vcc, v3, v2
	v_add_u32_e32 v3, 1, v5
	s_nop 0
	v_cndmask_b32_e32 v1, v1, v4, vcc
	v_mul_lo_u32 v4, v2, v1
	v_add_u32_e32 v2, v4, v2
	v_cmp_ne_u32_e32 vcc, v3, v2
	s_and_saveexec_b64 s[4:5], vcc
	s_xor_b64 s[4:5], exec, s[4:5]
	s_cbranch_execz .LBB0_1810
	s_waitcnt lgkmcnt(0)
	v_mad_u32_u24 v3, v1, v0, v0
	v_mov_b32_e32 v0, 0x3400
	global_load_dword v0, v0, s[30:31] sc1
	s_add_u32 s8, s30, 0x3400
	s_addc_u32 s9, s31, 0
	s_waitcnt vmcnt(0)
	v_cmp_lt_u32_e32 vcc, v0, v3
	s_and_saveexec_b64 s[6:7], vcc
	s_cbranch_execz .LBB0_1809
	s_mov_b32 s20, 1
	s_mov_b64 s[10:11], 0
	v_mov_b32_e32 v0, 0
	s_branch .LBB0_1800

; __device__ __forceinline__ unsigned xb_ld(unsigned* p)              { return __hip_atomic_load(p, __ATOMIC_RELAXED, __HIP_MEMORY_SCOPE_AGENT); }
; #define XB_SPIN(cond, bar) do { unsigned _sp = 0; while (cond) { __builtin_amdgcn_s_sleep(1); \
;     if ((++_sp & 255u) == 0u) { if (xb_ld(&(bar)[XB_TMO])) break; if (_sp > XB_SPIN_CAP) { atomicAdd(&(bar)[XB_TMO], 1u); break; } } } } while (0)
; __device__ __forceinline__ void xcd_barrier(const XcdBarrier& b) {
;     ...
;             else XB_SPIN(xb_ld(&bar[XB_TOPGEN]) == tg, bar);
.LBB0_1804:
	global_load_dword v2, v0, s[8:9] sc1
	s_add_i32 s20, s20, 1
	s_mov_b64 s[16:17], -1
	s_waitcnt vmcnt(0)
	v_cmp_ge_u32_e32 vcc, v2, v3
	s_orn2_b64 s[14:15], vcc, exec
	s_branch .LBB0_1799

; __device__ __forceinline__ unsigned xb_ld(unsigned* p)              { return __hip_atomic_load(p, __ATOMIC_RELAXED, __HIP_MEMORY_SCOPE_AGENT); }
; __device__ __forceinline__ unsigned xb_add(unsigned* p, unsigned v) { return __hip_atomic_fetch_add(p, v, __ATOMIC_RELAXED, __HIP_MEMORY_SCOPE_AGENT); }
; #define XB_SPIN(cond, bar) do { unsigned _sp = 0; while (cond) { __builtin_amdgcn_s_sleep(1); \
;     if ((++_sp & 255u) == 0u) { if (xb_ld(&(bar)[XB_TMO])) break; if (_sp > XB_SPIN_CAP) { atomicAdd(&(bar)[XB_TMO], 1u); break; } } } } while (0)
; __device__ __forceinline__ void xcd_barrier(const XcdBarrier& b) {
;     ...
;         const unsigned old = xb_add(&bar[XB_XSUB(b.x)], 1u);
;         const unsigned gen = old / nloc;
;         if (old + 1u == (gen + 1u) * nloc) {
;             __builtin_amdgcn_fence(__ATOMIC_RELEASE, "agent");
;             asm volatile("s_waitcnt vmcnt(0)" ::: "memory");
;             const unsigned og = xb_add(&bar[XB_TOP], 1u);
;             const unsigned tg = og / nx;
;             if (og + 1u == (tg + 1u) * nx) xb_add(&bar[XB_TOPGEN], 1u);
;             else XB_SPIN(xb_ld(&bar[XB_TOPGEN]) == tg, bar);
;             __builtin_amdgcn_fence(__ATOMIC_ACQUIRE, "agent");
;             xb_add(&bar[XB_XGEN(b.x)], 1u);
;             asm volatile("s_waitcnt vmcnt(0)" ::: "memory");
.LBB0_1813:
	s_or_b64 exec, exec, s[6:7]
	v_cvt_f32_u32_e32 v3, v0
	s_waitcnt vmcnt(0)
	v_readfirstlane_b32 s4, v2
	s_add_u32 s6, s30, 0x3400
	s_addc_u32 s7, s31, 0
	v_rcp_iflag_f32_e32 v3, v3
	v_add_u32_e32 v1, s4, v1
	v_add_u32_e32 v4, 1, v1
	s_mov_b64 s[8:9], -1
	v_mul_f32_e32 v2, 0x4f7ffffe, v3
	v_cvt_u32_f32_e32 v2, v2
	v_sub_u32_e32 v3, 0, v0
	v_mul_lo_u32 v3, v3, v2
	v_mul_hi_u32 v3, v2, v3
	v_add_u32_e32 v2, v2, v3
	v_mul_hi_u32 v2, v1, v2
	v_mul_lo_u32 v3, v2, v0
	v_sub_u32_e32 v1, v1, v3
	v_add_u32_e32 v5, 1, v2
	v_cmp_ge_u32_e32 vcc, v1, v0
	v_sub_u32_e32 v3, v1, v0
	s_nop 0
	v_cndmask_b32_e32 v2, v2, v5, vcc
	v_cndmask_b32_e32 v1, v1, v3, vcc
	v_add_u32_e32 v3, 1, v2
	v_cmp_ge_u32_e32 vcc, v1, v0
	s_nop 1
	v_cndmask_b32_e32 v2, v2, v3, vcc
	v_mul_lo_u32 v1, v0, v2
	v_add_u32_e32 v0, v1, v0
	v_mov_b32_e32 v6, v0
	v_cmp_ne_u32_e32 vcc, v4, v0
	v_mov_b64_e32 v[0:1], s[6:7]
	s_and_saveexec_b64 s[4:5], vcc
	s_cbranch_execz .LBB0_1825
	v_mov_b32_e32 v0, 0
	global_load_dword v1, v0, s[6:7] sc1
	s_mov_b64 s[12:13], 0
	s_waitcnt vmcnt(0)
	v_cmp_lt_u32_e32 vcc, v1, v6
	s_and_saveexec_b64 s[10:11], vcc
	s_cbranch_execz .LBB0_1824
	s_add_u32 s8, s30, 0x200
	s_addc_u32 s9, s31, 0
	s_mov_b32 s22, 1
	s_branch .LBB0_1817

; __device__ __forceinline__ unsigned xb_ld(unsigned* p)              { return __hip_atomic_load(p, __ATOMIC_RELAXED, __HIP_MEMORY_SCOPE_AGENT); }
; #define XB_SPIN(cond, bar) do { unsigned _sp = 0; while (cond) { __builtin_amdgcn_s_sleep(1); \
;     if ((++_sp & 255u) == 0u) { if (xb_ld(&(bar)[XB_TMO])) break; if (_sp > XB_SPIN_CAP) { atomicAdd(&(bar)[XB_TMO], 1u); break; } } } } while (0)
; __device__ __forceinline__ void xcd_barrier(const XcdBarrier& b) {
;     ...
;             else XB_SPIN(xb_ld(&bar[XB_TOPGEN]) == tg, bar);
.LBB0_1821:
	global_load_dword v1, v0, s[6:7] sc1
	s_add_i32 s22, s22, 1
	s_mov_b64 s[16:17], -1
	s_waitcnt vmcnt(0)
	v_cmp_ge_u32_e32 vcc, v1, v6
	s_orn2_b64 s[20:21], vcc, exec
	s_branch .LBB0_1816

; __device__ __forceinline__ unsigned xb_ld(unsigned* p)              { return __hip_atomic_load(p, __ATOMIC_RELAXED, __HIP_MEMORY_SCOPE_AGENT); }
; __device__ __forceinline__ unsigned xb_add(unsigned* p, unsigned v) { return __hip_atomic_fetch_add(p, v, __ATOMIC_RELAXED, __HIP_MEMORY_SCOPE_AGENT); }
; #define XB_SPIN(cond, bar) do { unsigned _sp = 0; while (cond) { __builtin_amdgcn_s_sleep(1); \
;     if ((++_sp & 255u) == 0u) { if (xb_ld(&(bar)[XB_TMO])) break; if (_sp > XB_SPIN_CAP) { atomicAdd(&(bar)[XB_TMO], 1u); break; } } } } while (0)
; __device__ __forceinline__ void xcd_barrier(const XcdBarrier& b) {
;     ...
;             const unsigned og = xb_add(&bar[XB_TOP], 1u);
;             const unsigned tg = og / nx;
;             if (og + 1u == (tg + 1u) * nx) xb_add(&bar[XB_TOPGEN], 1u);
;             else XB_SPIN(xb_ld(&bar[XB_TOPGEN]) == tg, bar);
;             __builtin_amdgcn_fence(__ATOMIC_ACQUIRE, "agent");
;             xb_add(&bar[XB_XGEN(b.x)], 1u);
.LBB0_1825:
	s_or_b64 exec, exec, s[4:5]
	s_and_saveexec_b64 s[4:5], s[8:9]
	s_cbranch_execz .LBB0_1827
.LBB0_1827:
	s_or_b64 exec, exec, s[4:5]
	s_waitcnt vmcnt(0)
	buffer_inv sc1
	s_waitcnt vmcnt(0)
